# convpool-tail idle workgroups convert 3 MoE weight tiles each (was 2)
# speedup vs baseline: 1.0162x; 1.0024x over previous
; #define LAS __attribute__((address_space(3)))
; __device__ __forceinline__ void tr_slack(const Ctx& P, LAS unsigned char* lds, unsigned* tilectr, unsigned* cnt, unsigned target) {
;     const int tid = threadIdx.x, lane = tid & 63, wave = __builtin_amdgcn_readfirstlane(tid >> 6);
;     volatile LAS int* box = (volatile LAS int*)(lds + LDS_MISC + 2048);
;     int r = -1; unsigned pollv = 0u;
;     if (tid == 0) { int stop0 = 0; if (cnt) stop0 = (__hip_atomic_load(cnt, __ATOMIC_RELAXED, __HIP_MEMORY_SCOPE_AGENT) >= target) ? 1 : 0;
;         box[0] = stop0 ? -1 : (int)__hip_atomic_fetch_add(tilectr, 1u, __ATOMIC_RELAXED, __HIP_MEMORY_SCOPE_AGENT); box[1] = stop0; }
;     __syncthreads();
;     int idx = box[0], stop = box[1];
;     const int sw = lane & 7;
;     while (idx >= 0 && idx < TR_NMOE) {
; __device__ __forceinline__ void phase_convpool(const Ctx& P, LAS unsigned char* lds, int vcu, int G) {
;     ...
;     constexpr int NU = 4 * 128 + 4 * 8;
;     for (int un = vcu; un < NU; un += G) {
.Lp3_tail_d:
	s_cmp_lt_u32 s33, s100
	s_cbranch_scc1 .LBB0_1122
	s_mov_b64 s[28:29], s[0:1]
	s_mov_b32 s100, 3
	s_mov_b32 s101, 1
	s_branch .Ltf1
